# stack10 with the up-GEMM K-loop moved by 4 B so its 8-byte MFMA encodings sit on 8-byte boundaries (down restored by another 4 B)
# baseline (speedup 1.0000x reference)
; #define PG8_STAGE(bufoff, gbase, voff) do { _Pragma("unroll") for (int _i = 0; _i < 2; ++_i) \
;         __builtin_amdgcn_global_load_lds((const unsigned*)((const char*)(gbase) + (voff)[_i]), (PG8_LAS unsigned*)(lds + (bufoff) + ldsw + _i * 8192), 16, 0, 0); } while (0)
; #define PG8_WAIT_V(n) asm volatile("s_waitcnt vmcnt(" #n ")" ::: "memory")
; #define PG8_BAR __builtin_amdgcn_s_barrier()
; template <class Epi, class Sched, bool ALIGN_EPI = false, bool SP2 = false>
; __device__ __forceinline__ void gemm_phase(PG8_LAS unsigned char* lds, const Gemm g, const Sched& S, const Epi& E, Stopwatch& sw) {
;     ...
;     for (int i = 0; i < 2; ++i) { int R, C; stage_rc(tid * 16 + i * 8192, R, C); const int Rb = Epi::PERM ? ((R & ~31) + perm32(R & 31)) : R;
;         voffA[i] = (unsigned)(R * K + C) * 2u; voffB[i] = (unsigned)(Rb * K + C) * 2u; }
;     const size_t kstep = (size_t)(BK * 2);
;     const size_t hstep = (size_t)HALF * K * 2;
;     const size_t tstep = 2 * hstep;
;     const unsigned ldsw = (unsigned)wid * 1024u;
;     const int aoff = lds_byte(wr * 64 + fr, fq * 8), boff = lds_byte(wc * 32 + fr, fq * 8);
;     ...
;     if constexpr (SP2) {
;         PG8_STAGE(PG8_SB(0, 0), cB, voffB); PG8_STAGE(PG8_SB(0, 1), cB + hstep, voffB); PG8_STAGE(PG8_SA(0, 0), cA, voffA); PG8_STAGE(PG8_SA(0, 1), cA + hstep, voffA);
;         if (wr == 1) PG8_BAR;
;         PG8_WAIT_V(2); PG8_BAR;
;         PG8_STAGE(PG8_SB(1, 0), cB + kstep, voffB); PG8_STAGE(PG8_SA(1, 0), cA + kstep, voffA); PG8_STAGE(PG8_SB(1, 1), cB + hstep + kstep, voffB);
.LBB0_1103:
	s_nop 0
	s_cmp_le_i32 s86, s0
	s_cselect_b64 s[4:5], -1, 0
	s_cmp_lt_i32 s0, s87
	v_readlane_b32 s0, v255, 26
	s_cselect_b64 s[18:19], -1, 0
	s_lshl_b32 s36, s0, 24
	v_readlane_b32 s0, v255, 27
	s_and_b64 s[18:19], s[4:5], s[18:19]
	s_add_i32 s5, s0, 9
	s_cmp_lt_i32 s5, s87
	s_cselect_b64 s[42:43], -1, 0
	s_andn2_b64 vcc, exec, s[18:19]
	s_cbranch_vccnz .LBB0_1213
	v_readlane_b32 s18, v253, 46
	s_waitcnt vmcnt(0)
	v_mov_b32_e32 v14, v234
	v_readlane_b32 s19, v253, 47
	s_andn2_b64 vcc, exec, s[18:19]
	v_readfirstlane_b32 s0, v14
	s_cbranch_vccnz .LBB0_1138
	v_lshlrev_b32_e32 v1, 4, v14
	v_add_u32_e32 v2, 0x2000, v1
	s_waitcnt lgkmcnt(0)
	v_ashrrev_i32_e32 v4, 31, v2
	v_lshrrev_b32_e32 v4, 22, v4
	v_add_u32_e32 v4, v2, v4
	v_ashrrev_i32_e32 v8, 10, v4
	v_mul_i32_i24_e32 v4, 0x400, v8
	v_sub_u32_e32 v2, v2, v4
	v_lshrrev_b32_e32 v4, 4, v2
	v_bitop3_b32 v2, v4, v2, 32 bitop3:0x6c
	v_ashrrev_i32_e32 v4, 31, v2
	v_lshrrev_b32_e32 v4, 26, v4
	v_add_u32_e32 v4, v2, v4
	v_lshlrev_b32_e32 v5, 3, v8
	v_ashrrev_i32_e32 v9, 6, v4
	v_and_b32_e32 v5, -16, v5
	v_add_u32_e32 v5, v9, v5
	v_and_b32_e32 v6, 3, v9
	s_mov_b32 s24, 0x1fffe0
	v_lshrrev_b32_e32 v7, 2, v5
	v_lshlrev_b32_e32 v10, 1, v5
	v_and_b32_e32 v4, 0xc0, v4
	v_and_or_b32 v6, v5, s24, v6
	v_and_b32_e32 v7, 4, v7
	v_and_b32_e32 v10, 24, v10
	v_sub_u32_e32 v2, v2, v4
	v_or3_b32 v6, v6, v7, v10
	v_lshlrev_b32_e32 v7, 5, v8
	v_ashrrev_i16_sdwa v2, v235, sext(v2) dst_sel:DWORD dst_unused:UNUSED_PAD src0_sel:DWORD src1_sel:BYTE_0
	v_and_b32_e32 v7, 32, v7
	v_bfe_i32 v10, v2, 0, 16
	v_add_lshl_u32 v2, v7, v10, 1
	v_lshl_add_u32 v196, v6, 11, v2
	v_lshl_add_u32 v202, v5, 11, v2
	v_bfe_i32 v2, v14, 27, 1
	v_lshrrev_b32_e32 v2, 22, v2
	v_add_u32_e32 v2, v1, v2
	v_and_b32_e32 v2, 0xfffffc00, v2
	v_sub_u32_e32 v1, v1, v2
	v_lshrrev_b32_e32 v2, 4, v1
	v_ashrrev_i32_e32 v4, 31, v14
	v_bitop3_b32 v1, v2, v1, 32 bitop3:0x6c
	v_lshrrev_b32_e32 v4, 26, v4
	v_ashrrev_i32_e32 v2, 31, v1
	v_add_u32_e32 v4, v14, v4
	v_lshrrev_b32_e32 v2, 26, v2
	v_ashrrev_i32_e32 v12, 6, v4
	v_add_u32_e32 v2, v1, v2
	v_lshlrev_b32_e32 v4, 3, v12
	s_ashr_i32 s3, s0, 6
	v_ashrrev_i32_e32 v11, 6, v2
	v_and_b32_e32 v4, -16, v4
	s_ashr_i32 s4, s0, 8
	s_lshl_b32 s19, s3, 10
	v_readlane_b32 s16, v250, 28
	v_add_u32_e32 v4, v11, v4
	s_add_u32 s16, s16, s36
	v_readlane_b32 s18, v250, 29
	v_and_b32_e32 v5, 3, v11
	v_lshrrev_b32_e32 v6, 2, v4
	v_lshlrev_b32_e32 v7, 1, v4
	v_and_b32_e32 v2, 0xc0, v2
	s_addc_u32 s18, s18, 0
	v_and_or_b32 v5, v4, s24, v5
	v_and_b32_e32 v6, 4, v6
	v_and_b32_e32 v7, 24, v7
	v_sub_u32_e32 v1, v1, v2
	v_readlane_b32 s24, v254, 9
	v_writelane_b32 v255, s56, 28
	v_or3_b32 v5, v5, v6, v7
	v_lshlrev_b32_e32 v6, 5, v12
	v_ashrrev_i16_sdwa v1, v235, sext(v1) dst_sel:DWORD dst_unused:UNUSED_PAD src0_sel:DWORD src1_sel:BYTE_0
	v_readlane_b32 s25, v254, 10
	s_add_u32 s40, s16, s24
	v_writelane_b32 v255, s57, 29
	v_and_b32_e32 v6, 32, v6
	v_bfe_i32 v13, v1, 0, 16
	s_addc_u32 s41, s18, s25
	s_add_i32 s19, s19, 0
	v_writelane_b32 v255, s36, 30
	v_add_lshl_u32 v1, v6, v13, 1
	s_add_i32 s25, s19, 0x10000
	s_add_i32 s36, s19, 0x12000
	v_lshl_add_u32 v2, v5, 11, v1
	s_mov_b32 m0, s25
	s_add_u32 s38, s40, 0x40000
	global_load_lds_dwordx4 v2, s[40:41]
	s_mov_b32 m0, s36
	s_addc_u32 s39, s41, 0
	s_add_i32 s37, s19, 0x14000
	global_load_lds_dwordx4 v196, s[40:41]
	s_mov_b32 m0, s37
	s_add_i32 s72, s19, 0x16000
	global_load_lds_dwordx4 v2, s[38:39]
	s_mov_b32 m0, s72
	v_lshl_add_u32 v204, v4, 11, v1
	global_load_lds_dwordx4 v196, s[38:39]
	v_readlane_b32 s38, v254, 15
	s_mov_b32 m0, s19
	v_readlane_b32 s39, v254, 16
	s_add_i32 s73, s19, 0x2000
	s_add_i32 s80, s19, 0x4000
	s_add_i32 s81, s19, 0x6000
	v_mov_b32_e32 v197, v3
	s_cmp_eq_u32 s4, 1
	global_load_lds_dwordx4 v204, s[38:39]
	s_mov_b32 m0, s73
	v_lshl_add_u64 v[4:5], s[40:41], 0, v[2:3]
	global_load_lds_dwordx4 v202, s[38:39]
	v_readlane_b32 s38, v254, 17
	s_mov_b32 m0, s80
	v_readlane_b32 s39, v254, 18
	s_cselect_b64 s[44:45], -1, 0
	s_cmp_lg_u32 s4, 1
	v_lshl_add_u64 v[6:7], s[40:41], 0, v[196:197]
	s_nop 1
	global_load_lds_dwordx4 v204, s[38:39]
	s_mov_b32 m0, s81
	s_nop 0
	global_load_lds_dwordx4 v202, s[38:39]
	s_cbranch_scc1 .LBB0_1107
	s_barrier

; #define PG8_STAGE(bufoff, gbase, voff) do { _Pragma("unroll") for (int _i = 0; _i < 2; ++_i) \
;         __builtin_amdgcn_global_load_lds((const unsigned*)((const char*)(gbase) + (voff)[_i]), (PG8_LAS unsigned*)(lds + (bufoff) + ldsw + _i * 8192), 16, 0, 0); } while (0)
; #define PG8_WAIT_V(n) asm volatile("s_waitcnt vmcnt(" #n ")" ::: "memory")
; #define PG8_BAR __builtin_amdgcn_s_barrier()
; template <class Epi, class Sched, bool ALIGN_EPI = false, bool SP2 = false>
; __device__ __forceinline__ void gemm_phase(PG8_LAS unsigned char* lds, const Gemm g, const Sched& S, const Epi& E, Stopwatch& sw) {
;     ...
;     const int tid = tid_, wid = __builtin_amdgcn_readfirstlane(tid >> 6), lane = tid & 63, wr = wid >> 2, wc = wid & 3, fr = lane & 15, fq = lane >> 4;
;     const int K = g.K, nt = K / BK;
;     unsigned voffA[2], voffB[2];
; #pragma unroll
;     for (int i = 0; i < 2; ++i) { int R, C; stage_rc(tid * 16 + i * 8192, R, C); const int Rb = Epi::PERM ? ((R & ~31) + perm32(R & 31)) : R;
;         voffA[i] = (unsigned)(R * K + C) * 2u; voffB[i] = (unsigned)(Rb * K + C) * 2u; }
;     const size_t kstep = (size_t)(BK * 2);
;     const size_t hstep = (size_t)HALF * K * 2;
;     const size_t tstep = 2 * hstep;
;     const unsigned ldsw = (unsigned)wid * 1024u;
;     const int aoff = lds_byte(wr * 64 + fr, fq * 8), boff = lds_byte(wc * 32 + fr, fq * 8);
;     ...
;     const char* cA = (const char*)g.A + (size_t)cur.pm * tstep; const char* cB = (const char*)g.Bt + (size_t)cur.pn * tstep;
;     S.a_ready(cur);
;     if constexpr (SP2) {
;         PG8_STAGE(PG8_SB(0, 0), cB, voffB); PG8_STAGE(PG8_SB(0, 1), cB + hstep, voffB); PG8_STAGE(PG8_SA(0, 0), cA, voffA); PG8_STAGE(PG8_SA(0, 1), cA + hstep, voffA);
;         if (wr == 1) PG8_BAR;
;         PG8_WAIT_V(2); PG8_BAR;
.LBB0_1213:
	s_nop 0
	s_cmp_le_i32 s86, s5
	s_cselect_b64 s[4:5], -1, 0
	s_and_b64 s[42:43], s[4:5], s[42:43]
	s_andn2_b64 vcc, exec, s[42:43]
	s_cbranch_vccnz .LBB0_1264
	s_waitcnt vmcnt(0) lgkmcnt(0)
	v_mov_b32_e32 v4, v234
	s_and_b64 vcc, exec, s[56:57]
	v_readfirstlane_b32 s0, v4
	s_cbranch_vccnz .LBB0_1264
	v_lshlrev_b32_e32 v1, 4, v4
	v_add_u32_e32 v2, 0x2000, v1
	v_ashrrev_i32_e32 v5, 31, v2
	v_lshrrev_b32_e32 v5, 22, v5
	v_add_u32_e32 v5, v2, v5
	v_ashrrev_i32_e32 v5, 10, v5
	v_mul_i32_i24_e32 v6, 0x400, v5
	v_sub_u32_e32 v2, v2, v6
	v_lshrrev_b32_e32 v6, 4, v2
	v_bitop3_b32 v2, v6, v2, 32 bitop3:0x6c
	v_ashrrev_i32_e32 v6, 31, v2
	v_lshrrev_b32_e32 v6, 26, v6
	v_add_u32_e32 v7, v2, v6
	v_lshlrev_b32_e32 v8, 3, v5
	v_ashrrev_i32_e32 v6, 6, v7
	v_and_b32_e32 v8, -16, v8
	v_add_u32_e32 v8, v6, v8
	v_and_b32_e32 v9, 3, v6
	s_mov_b32 s18, 0x3ffe0
	v_lshrrev_b32_e32 v10, 2, v8
	v_lshlrev_b32_e32 v11, 1, v8
	v_and_b32_e32 v7, 0xc0, v7
	v_and_or_b32 v9, v8, s18, v9
	v_and_b32_e32 v10, 4, v10
	v_and_b32_e32 v11, 24, v11
	v_sub_u32_e32 v2, v2, v7
	v_or3_b32 v9, v9, v10, v11
	v_lshlrev_b32_e32 v10, 5, v5
	v_ashrrev_i16_sdwa v2, v235, sext(v2) dst_sel:DWORD dst_unused:UNUSED_PAD src0_sel:DWORD src1_sel:BYTE_0
	v_and_b32_e32 v10, 32, v10
	v_bfe_i32 v7, v2, 0, 16
	v_add_lshl_u32 v2, v10, v7, 1
	v_lshl_add_u32 v196, v9, 14, v2
	v_lshl_add_u32 v202, v8, 14, v2
	v_bfe_i32 v2, v4, 27, 1
	v_lshrrev_b32_e32 v2, 22, v2
	v_add_u32_e32 v2, v1, v2
	v_and_b32_e32 v2, 0xfffffc00, v2
	v_sub_u32_e32 v1, v1, v2
	v_lshrrev_b32_e32 v2, 4, v1
	v_ashrrev_i32_e32 v9, 31, v4
	v_bitop3_b32 v1, v2, v1, 32 bitop3:0x6c
	v_lshrrev_b32_e32 v9, 26, v9
	v_ashrrev_i32_e32 v2, 31, v1
	v_add_u32_e32 v9, v4, v9
	v_lshrrev_b32_e32 v2, 26, v2
	v_ashrrev_i32_e32 v9, 6, v9
	v_add_u32_e32 v2, v1, v2
	v_lshlrev_b32_e32 v10, 3, v9
	s_ashr_i32 s34, s0, 6
	v_ashrrev_i32_e32 v8, 6, v2
	v_and_b32_e32 v10, -16, v10
	s_ashr_i32 s3, s0, 8
	s_lshl_b32 s16, s34, 10
	s_lshl_b32 s4, s36, 1
	v_readlane_b32 s5, v250, 22
	v_add_u32_e32 v11, v8, v10
	s_add_u32 s4, s5, s4
	v_readlane_b32 s5, v250, 23
	v_and_b32_e32 v10, 3, v8
	v_lshrrev_b32_e32 v12, 2, v11
	v_lshlrev_b32_e32 v13, 1, v11
	v_and_b32_e32 v2, 0xc0, v2
	s_addc_u32 s5, s5, 0
	v_and_or_b32 v10, v11, s18, v10
	v_and_b32_e32 v12, 4, v12
	v_and_b32_e32 v13, 24, v13
	v_sub_u32_e32 v1, v1, v2
	v_readlane_b32 s18, v254, 19
	v_or3_b32 v12, v10, v12, v13
	v_lshlrev_b32_e32 v10, 5, v9
	v_ashrrev_i16_sdwa v1, v235, sext(v1) dst_sel:DWORD dst_unused:UNUSED_PAD src0_sel:DWORD src1_sel:BYTE_0
	v_readlane_b32 s19, v254, 20
	s_add_u32 s40, s4, s18
	v_and_b32_e32 v13, 32, v10
	v_bfe_i32 v10, v1, 0, 16
	s_addc_u32 s41, s5, s19
	v_readlane_b32 s100, v254, 21
	v_readlane_b32 s101, v253, 53
	s_nop 0
	s_and_b32 s18, s100, 7
	s_andn2_b32 s100, s100, 7
	s_add_i32 s100, s100, s101
	s_mov_b32 s101, s18
	s_lshl_b32 s19, s18, 22
	s_add_u32 s40, s4, s19
	s_addc_u32 s41, s5, 0
	s_add_i32 s16, s16, 0
	v_add_lshl_u32 v1, v13, v10, 1
	s_add_i32 s18, s16, 0x10000
	s_add_i32 s19, s16, 0x12000
	v_lshl_add_u32 v2, v12, 14, v1
	s_mov_b32 m0, s18
	s_add_u32 s36, s40, 0x200000
	global_load_lds_dwordx4 v2, s[40:41]
	s_mov_b32 m0, s19
	s_addc_u32 s37, s41, 0
	s_add_i32 s24, s16, 0x14000
	global_load_lds_dwordx4 v196, s[40:41]
	s_mov_b32 m0, s24
	s_add_i32 s25, s16, 0x16000
	global_load_lds_dwordx4 v2, s[36:37]
	s_mov_b32 m0, s25
	v_lshl_add_u32 v204, v11, 14, v1
	global_load_lds_dwordx4 v196, s[36:37]
	s_lshl_b32 s36, s100, 22
	s_add_u32 s36, s14, s36
	s_mov_b32 m0, s16
	s_addc_u32 s37, s15, 0
	s_add_u32 s98, s36, 0x200000
	s_addc_u32 s99, s37, 0
	s_add_i32 s31, s16, 0x2000
	s_add_i32 s72, s16, 0x4000
	s_add_i32 s73, s16, 0x6000
	s_cmp_eq_u32 s3, 1
	s_cselect_b64 s[44:45], -1, 0
	global_load_lds_dwordx4 v204, s[36:37]
	s_mov_b32 m0, s31
	s_cmp_lg_u32 s3, 1
	global_load_lds_dwordx4 v202, s[36:37]
	s_mov_b32 s36, s98
	s_mov_b32 m0, s72
	s_mov_b32 s37, s99
	s_nop 4
	global_load_lds_dwordx4 v204, s[36:37]
	s_mov_b32 m0, s73
	s_nop 0
	global_load_lds_dwordx4 v202, s[36:37]
	s_cbranch_scc1 .LBB0_1217
	s_barrier
